# prep phase: adaLN partial tasks split 4:2 between lower-half and upper-half workgroups (upper half spends the start of the phase on the WcsT fold)
# speedup vs baseline: 1.0122x; 1.0062x over previous
; __device__ __forceinline__ float silu_f(float v) { return v / (1.f + __expf(-v)); }
; __device__ void adaln_partial_task(KParams& p, int task, float* sm) {
;   const int cb = task % 48, ks = task / 48, tid = threadIdx.x;
;   float* sc = sm;
;   __syncthreads();
;   for (int i = tid; i < 5 * 64; i += NTHREADS) {
;     int r = i >> 6, kk = i & 63;
;     int k = ks * 64 + kk;
;     float cv = (r < 4) ? p.c[r * D + k] : p.c_ctx[k];
;     sc[i] = silu_f(cv);
;   }
;   __syncthreads();
;   const int col = cb * 256 + tid;
;   float a0 = 0, a1 = 0, a2 = 0, a3 = 0, a4 = 0;
;   const float* wp = p.w_mod + (size_t)(ks * 64) * NMOD + col;
;   {
;     float wv[64];
; #pragma unroll
;     for (int kk = 0; kk < 64; ++kk) wv[kk] = __builtin_nontemporal_load(wp + (size_t)kk * NMOD);
; #pragma unroll
;     for (int k = 0; k < 64; ++k) {
;       a0 += sc[k] * wv[k]; a1 += sc[64 + k] * wv[k]; a2 += sc[128 + k] * wv[k]; a3 += sc[192 + k] * wv[k]; a4 += sc[256 + k] * wv[k];
;     }
;   }
;   float* pp = p.partial + (size_t)ks * 5 * NMOD + col;
;   pp[0] = a0; pp[NMOD] = a1; pp[2 * NMOD] = a2; pp[3 * NMOD] = a3; pp[4 * NMOD] = a4;
; __device__ void phase_prep(KParams& p, int bid, int nb, char* smem) {
;     ...
;   for (int t = bid; t < 48 * KSPLIT; t += nb) adaln_partial_task(p, t, sm);
.Lmy_A:
	s_mov_b32 s90, s2
	s_mov_b32 s100, s34
	s_movk_i32 s101, 0x5ff
	s_cmpk_lg_u32 s34, 0x200
	s_cbranch_scc1 .Lmy_A2
	s_movk_i32 s100, 0x100
	s_movk_i32 s101, 1023
	s_cmp_eq_u32 s99, 0
	s_cbranch_scc1 .Lmy_A2
	s_add_u32 s90, s2, 768
	s_movk_i32 s101, 0x5ff
.Lmy_A2:
	s_cmp_gt_i32 s90, s101
	s_cbranch_scc1 .LBB0_19
	s_load_dwordx2 s[14:15], s[12:13], 0x8
	s_load_dwordx4 s[8:11], s[12:13], 0x18
	s_load_dwordx2 s[16:17], s[12:13], 0x180
	s_movk_i32 s3, 0x140
	v_cmp_gt_u32_e64 s[6:7], s3, v0
	v_lshlrev_b32_e32 v1, 5, v0
	s_movk_i32 s3, 0x100
	s_mov_b32 s22, 0xc000
	s_mov_b32 s23, 0x18000
	s_mov_b32 s24, 0x24000
	s_mov_b32 s25, 0x30000
	s_mov_b32 s26, 0x3c000
	s_mov_b32 s27, 0x48000
	s_mov_b32 s28, 0x54000
	s_mov_b32 s29, 0x60000
	s_mov_b32 s30, 0x6c000
	s_mov_b32 s31, 0x78000
	s_mov_b32 s35, 0x84000
	s_mov_b32 s36, 0x90000
	s_mov_b32 s37, 0x9c000
	s_mov_b32 s38, 0xa8000
	s_mov_b32 s39, 0xb4000
	s_mov_b32 s40, 0xc0000
	s_mov_b32 s41, 0xcc000
	s_mov_b32 s42, 0xd8000
	s_mov_b32 s43, 0xe4000
	s_mov_b32 s46, 0xf0000
	s_mov_b32 s47, 0xfc000
	s_mov_b32 s48, 0x108000
	s_mov_b32 s49, 0x114000
	s_mov_b32 s50, 0x120000
	s_mov_b32 s51, 0x12c000
	s_mov_b32 s52, 0x138000
	s_mov_b32 s53, 0x144000
	s_mov_b32 s54, 0x150000
	s_mov_b32 s55, 0x15c000
	s_mov_b32 s56, 0x168000
	s_mov_b32 s57, 0x174000
	s_mov_b32 s58, 0x180000
	s_mov_b32 s59, 0x18c000
	s_mov_b32 s60, 0x198000
	s_mov_b32 s61, 0x1a4000
	s_mov_b32 s62, 0x1b0000
	s_mov_b32 s63, 0x1bc000
	s_mov_b32 s64, 0x1c8000
	s_mov_b32 s65, 0x1d4000
	s_mov_b32 s66, 0x1e0000
	s_mov_b32 s67, 0x1ec000
	s_mov_b32 s68, 0x1f8000
	s_mov_b32 s69, 0x204000
	s_mov_b32 s70, 0x210000
	s_mov_b32 s71, 0x21c000
	s_mov_b32 s72, 0x228000
	s_mov_b32 s73, 0x234000
	s_mov_b32 s74, 0x240000
	s_mov_b32 s75, 0x24c000
	s_mov_b32 s76, 0x258000
	s_mov_b32 s77, 0x264000
	s_mov_b32 s78, 0x270000
	s_mov_b32 s79, 0x27c000
	s_mov_b32 s80, 0x288000
	s_mov_b32 s81, 0x294000
	s_mov_b32 s82, 0x2a0000
	s_mov_b32 s83, 0x2ac000
	s_mov_b32 s84, 0x2b8000
	s_mov_b32 s85, 0x2c4000
	s_mov_b32 s86, 0x2d0000
	s_mov_b32 s87, 0x2dc000
	s_mov_b32 s88, 0x2e8000
	s_mov_b32 s89, 0x2f4000
	v_mov_b32_e32 v6, 0
	s_branch .LBB0_16
.LBB0_15:
	s_or_b64 exec, exec, s[18:19]
	s_mul_i32 s18, s91, 48
	s_sub_i32 s18, s90, s18
	v_lshl_or_b32 v2, s18, 8, v0
	s_mul_hi_i32 s19, s92, 0xc000
	s_mul_i32 s92, s92, 0xc000
	s_add_u32 s18, s10, s92
	v_ashrrev_i32_e32 v3, 31, v2
	s_addc_u32 s19, s11, s19
	v_lshlrev_b64 v[2:3], 2, v[2:3]
	v_lshl_add_u64 v[4:5], s[18:19], 0, v[2:3]
	v_add_co_u32_e32 v8, vcc, s22, v4
	s_waitcnt lgkmcnt(0)
	s_nop 0
	v_addc_co_u32_e32 v9, vcc, 0, v5, vcc
	v_add_co_u32_e32 v10, vcc, s23, v4
	s_barrier
	s_nop 0
	v_addc_co_u32_e32 v11, vcc, 0, v5, vcc
	v_add_co_u32_e32 v12, vcc, s24, v4
	s_nop 1
	v_addc_co_u32_e32 v13, vcc, 0, v5, vcc
	v_add_co_u32_e32 v14, vcc, s25, v4
	s_mul_i32 s18, s91, 5
	s_nop 0
	v_addc_co_u32_e32 v15, vcc, 0, v5, vcc
	v_add_co_u32_e32 v16, vcc, s26, v4
	s_mul_i32 s91, s91, 0x3c000
	s_nop 0
	v_addc_co_u32_e32 v17, vcc, 0, v5, vcc
	v_add_co_u32_e32 v18, vcc, s27, v4
	s_mul_hi_i32 s19, s18, 0xc000
	s_nop 0
	v_addc_co_u32_e32 v19, vcc, 0, v5, vcc
	v_add_co_u32_e32 v20, vcc, s28, v4
	s_add_u32 s18, s16, s91
	s_nop 0
	v_addc_co_u32_e32 v21, vcc, 0, v5, vcc
	global_load_dword v114, v[4:5], off nt
	global_load_dword v115, v[8:9], off nt
	global_load_dword v116, v[10:11], off nt
	global_load_dword v117, v[12:13], off nt
	global_load_dword v118, v[14:15], off nt
	global_load_dword v119, v[16:17], off nt
	global_load_dword v120, v[18:19], off nt
	global_load_dword v121, v[20:21], off nt
	v_add_co_u32_e32 v8, vcc, s29, v4
	s_addc_u32 s19, s17, s19
	s_nop 0
	v_addc_co_u32_e32 v9, vcc, 0, v5, vcc
	v_add_co_u32_e32 v10, vcc, s30, v4
	v_lshl_add_u64 v[2:3], s[18:19], 0, v[2:3]
	s_nop 0
	v_addc_co_u32_e32 v11, vcc, 0, v5, vcc
	v_add_co_u32_e32 v12, vcc, s31, v4
	s_add_i32 s90, s90, s100
	s_nop 0
	v_addc_co_u32_e32 v13, vcc, 0, v5, vcc
	v_add_co_u32_e32 v14, vcc, s35, v4
	s_cmp_gt_i32 s90, s101
	s_nop 0
	v_addc_co_u32_e32 v15, vcc, 0, v5, vcc
	v_add_co_u32_e32 v16, vcc, s36, v4
	s_nop 1
	v_addc_co_u32_e32 v17, vcc, 0, v5, vcc
	v_add_co_u32_e32 v18, vcc, s37, v4
	s_nop 1
	v_addc_co_u32_e32 v19, vcc, 0, v5, vcc
	v_add_co_u32_e32 v20, vcc, s38, v4
	s_nop 1
	v_addc_co_u32_e32 v21, vcc, 0, v5, vcc
	v_add_co_u32_e32 v22, vcc, s39, v4
	s_nop 1
	v_addc_co_u32_e32 v23, vcc, 0, v5, vcc
	global_load_dword v65, v[8:9], off nt
	global_load_dword v64, v[10:11], off nt
	global_load_dword v63, v[12:13], off nt
	global_load_dword v62, v[14:15], off nt
	global_load_dword v61, v[16:17], off nt
	global_load_dword v60, v[18:19], off nt
	global_load_dword v59, v[20:21], off nt
	global_load_dword v58, v[22:23], off nt
	v_add_co_u32_e32 v8, vcc, s40, v4
	s_nop 1
	v_addc_co_u32_e32 v9, vcc, 0, v5, vcc
	v_add_co_u32_e32 v10, vcc, s41, v4
	s_nop 1
	v_addc_co_u32_e32 v11, vcc, 0, v5, vcc
	v_add_co_u32_e32 v12, vcc, s42, v4
	s_nop 1
	v_addc_co_u32_e32 v13, vcc, 0, v5, vcc
	v_add_co_u32_e32 v14, vcc, s43, v4
	s_nop 1
	v_addc_co_u32_e32 v15, vcc, 0, v5, vcc
	v_add_co_u32_e32 v16, vcc, s46, v4
	s_nop 1
	v_addc_co_u32_e32 v17, vcc, 0, v5, vcc
	v_add_co_u32_e32 v18, vcc, s47, v4
	s_nop 1
	v_addc_co_u32_e32 v19, vcc, 0, v5, vcc
	v_add_co_u32_e32 v20, vcc, s48, v4
	s_nop 1
	v_addc_co_u32_e32 v21, vcc, 0, v5, vcc
	v_add_co_u32_e32 v22, vcc, s49, v4
	s_nop 1
	v_addc_co_u32_e32 v23, vcc, 0, v5, vcc
	global_load_dword v57, v[8:9], off nt
	global_load_dword v56, v[10:11], off nt
	global_load_dword v55, v[12:13], off nt
	global_load_dword v54, v[14:15], off nt
	global_load_dword v53, v[16:17], off nt
	global_load_dword v52, v[18:19], off nt
	global_load_dword v51, v[20:21], off nt
; __device__ void adaln_partial_task(KParams& p, int task, float* sm) {
;     ...
;   const float* wp = p.w_mod + (size_t)(ks * 64) * NMOD + col;
;   {
;     float wv[64];
; #pragma unroll
;     for (int kk = 0; kk < 64; ++kk) wv[kk] = __builtin_nontemporal_load(wp + (size_t)kk * NMOD);
; #pragma unroll
;     for (int k = 0; k < 64; ++k) {
;       a0 += sc[k] * wv[k]; a1 += sc[64 + k] * wv[k]; a2 += sc[128 + k] * wv[k]; a3 += sc[192 + k] * wv[k]; a4 += sc[256 + k] * wv[k];
	global_load_dword v50, v[22:23], off nt
	v_add_co_u32_e32 v8, vcc, s50, v4
	s_nop 1
	v_addc_co_u32_e32 v9, vcc, 0, v5, vcc
	v_add_co_u32_e32 v10, vcc, s51, v4
	s_nop 1
	v_addc_co_u32_e32 v11, vcc, 0, v5, vcc
	v_add_co_u32_e32 v12, vcc, s52, v4
	s_nop 1
	v_addc_co_u32_e32 v13, vcc, 0, v5, vcc
	v_add_co_u32_e32 v14, vcc, s53, v4
	s_nop 1
	v_addc_co_u32_e32 v15, vcc, 0, v5, vcc
	v_add_co_u32_e32 v16, vcc, s54, v4
	s_nop 1
	v_addc_co_u32_e32 v17, vcc, 0, v5, vcc
	v_add_co_u32_e32 v18, vcc, s55, v4
	s_nop 1
	v_addc_co_u32_e32 v19, vcc, 0, v5, vcc
	v_add_co_u32_e32 v20, vcc, s56, v4
	s_nop 1
	v_addc_co_u32_e32 v21, vcc, 0, v5, vcc
	v_add_co_u32_e32 v22, vcc, s57, v4
	s_nop 1
	v_addc_co_u32_e32 v23, vcc, 0, v5, vcc
	global_load_dword v49, v[8:9], off nt
	global_load_dword v48, v[10:11], off nt
	global_load_dword v47, v[12:13], off nt
	global_load_dword v46, v[14:15], off nt
	global_load_dword v45, v[16:17], off nt
	global_load_dword v44, v[18:19], off nt
	global_load_dword v43, v[20:21], off nt
	global_load_dword v42, v[22:23], off nt
	v_add_co_u32_e32 v8, vcc, s58, v4
	s_nop 1
	v_addc_co_u32_e32 v9, vcc, 0, v5, vcc
	v_add_co_u32_e32 v10, vcc, s59, v4
	s_nop 1
	v_addc_co_u32_e32 v11, vcc, 0, v5, vcc
	v_add_co_u32_e32 v12, vcc, s60, v4
	s_nop 1
	v_addc_co_u32_e32 v13, vcc, 0, v5, vcc
	v_add_co_u32_e32 v14, vcc, s61, v4
	s_nop 1
	v_addc_co_u32_e32 v15, vcc, 0, v5, vcc
	v_add_co_u32_e32 v16, vcc, s62, v4
	s_nop 1
	v_addc_co_u32_e32 v17, vcc, 0, v5, vcc
	v_add_co_u32_e32 v18, vcc, s63, v4
	s_nop 1
	v_addc_co_u32_e32 v19, vcc, 0, v5, vcc
	v_add_co_u32_e32 v20, vcc, s64, v4
	s_nop 1
	v_addc_co_u32_e32 v21, vcc, 0, v5, vcc
	v_add_co_u32_e32 v22, vcc, s65, v4
	s_nop 1
	v_addc_co_u32_e32 v23, vcc, 0, v5, vcc
	global_load_dword v41, v[8:9], off nt
	global_load_dword v40, v[10:11], off nt
	global_load_dword v39, v[12:13], off nt
	global_load_dword v38, v[14:15], off nt
	global_load_dword v37, v[16:17], off nt
	global_load_dword v36, v[18:19], off nt
	global_load_dword v35, v[20:21], off nt
	global_load_dword v34, v[22:23], off nt
	v_add_co_u32_e32 v8, vcc, s66, v4
	s_nop 1
	v_addc_co_u32_e32 v9, vcc, 0, v5, vcc
	v_add_co_u32_e32 v10, vcc, s67, v4
	s_nop 1
	v_addc_co_u32_e32 v11, vcc, 0, v5, vcc
	v_add_co_u32_e32 v12, vcc, s68, v4
	s_nop 1
	v_addc_co_u32_e32 v13, vcc, 0, v5, vcc
	v_add_co_u32_e32 v14, vcc, s69, v4
	s_nop 1
	v_addc_co_u32_e32 v15, vcc, 0, v5, vcc
	v_add_co_u32_e32 v16, vcc, s70, v4
	s_nop 1
	v_addc_co_u32_e32 v17, vcc, 0, v5, vcc
	v_add_co_u32_e32 v18, vcc, s71, v4
	s_nop 1
	v_addc_co_u32_e32 v19, vcc, 0, v5, vcc
	v_add_co_u32_e32 v20, vcc, s72, v4
	s_nop 1
	v_addc_co_u32_e32 v21, vcc, 0, v5, vcc
	v_add_co_u32_e32 v22, vcc, s73, v4
	s_nop 1
	v_addc_co_u32_e32 v23, vcc, 0, v5, vcc
	global_load_dword v33, v[8:9], off nt
	global_load_dword v32, v[10:11], off nt
	global_load_dword v31, v[12:13], off nt
	global_load_dword v30, v[14:15], off nt
	global_load_dword v29, v[16:17], off nt
	global_load_dword v28, v[18:19], off nt
	global_load_dword v27, v[20:21], off nt
	global_load_dword v26, v[22:23], off nt
	v_add_co_u32_e32 v8, vcc, s74, v4
	s_nop 1
	v_addc_co_u32_e32 v9, vcc, 0, v5, vcc
	v_add_co_u32_e32 v10, vcc, s75, v4
	s_nop 1
	v_addc_co_u32_e32 v11, vcc, 0, v5, vcc
	v_add_co_u32_e32 v12, vcc, s76, v4
	s_nop 1
	v_addc_co_u32_e32 v13, vcc, 0, v5, vcc
	v_add_co_u32_e32 v14, vcc, s77, v4
	s_nop 1
	v_addc_co_u32_e32 v15, vcc, 0, v5, vcc
	v_add_co_u32_e32 v16, vcc, s78, v4
	s_nop 1
	v_addc_co_u32_e32 v17, vcc, 0, v5, vcc
	v_add_co_u32_e32 v18, vcc, s79, v4
	s_nop 1
	v_addc_co_u32_e32 v19, vcc, 0, v5, vcc
	v_add_co_u32_e32 v66, vcc, s80, v4
	s_nop 1
	v_addc_co_u32_e32 v67, vcc, 0, v5, vcc
	v_add_co_u32_e32 v68, vcc, s81, v4
	s_nop 1
	v_addc_co_u32_e32 v69, vcc, 0, v5, vcc
	global_load_dword v25, v[8:9], off nt
	global_load_dword v24, v[10:11], off nt
	global_load_dword v23, v[12:13], off nt
	global_load_dword v22, v[14:15], off nt
	global_load_dword v21, v[16:17], off nt
	global_load_dword v20, v[18:19], off nt
	s_nop 0
	global_load_dword v19, v[66:67], off nt
	global_load_dword v18, v[68:69], off nt
	v_add_co_u32_e32 v8, vcc, s82, v4
	s_nop 1
	v_addc_co_u32_e32 v9, vcc, 0, v5, vcc
	v_add_co_u32_e32 v10, vcc, s83, v4
	s_nop 1
	v_addc_co_u32_e32 v11, vcc, 0, v5, vcc
	v_add_co_u32_e32 v12, vcc, s84, v4
	s_nop 1
	v_addc_co_u32_e32 v13, vcc, 0, v5, vcc
	v_add_co_u32_e32 v14, vcc, s85, v4
	s_nop 1
	v_addc_co_u32_e32 v15, vcc, 0, v5, vcc
	v_add_co_u32_e32 v66, vcc, s86, v4
	s_nop 1
	v_addc_co_u32_e32 v67, vcc, 0, v5, vcc
	v_add_co_u32_e32 v68, vcc, s87, v4
	s_nop 1
	v_addc_co_u32_e32 v69, vcc, 0, v5, vcc
	v_add_co_u32_e32 v70, vcc, s88, v4
	s_nop 1
	v_addc_co_u32_e32 v71, vcc, 0, v5, vcc
	v_add_co_u32_e32 v4, vcc, s89, v4
	s_nop 1
	v_addc_co_u32_e32 v5, vcc, 0, v5, vcc
	global_load_dword v17, v[8:9], off nt
	global_load_dword v16, v[10:11], off nt
	s_nop 0
	global_load_dword v13, v[12:13], off nt
	s_nop 0
	global_load_dword v11, v[14:15], off nt
	global_load_dword v9, v[66:67], off nt
	global_load_dword v8, v[68:69], off nt
	global_load_dword v7, v[70:71], off nt
	s_nop 0
	global_load_dword v4, v[4:5], off nt
	ds_read_b128 v[66:69], v6
	ds_read_b128 v[70:73], v6 offset:16
	ds_read_b128 v[74:77], v6 offset:256
	ds_read_b128 v[78:81], v6 offset:32
	ds_read_b128 v[82:85], v6 offset:48
	ds_read_b128 v[86:89], v6 offset:512
	ds_read_b128 v[90:93], v6 offset:272
	ds_read_b128 v[94:97], v6 offset:768
	ds_read_b128 v[98:101], v6 offset:1024
	ds_read_b128 v[102:105], v6 offset:528
	s_waitcnt vmcnt(62) lgkmcnt(9)
	v_fma_f32 v5, v114, v66, 0
	s_waitcnt lgkmcnt(7)
	v_fma_f32 v14, v114, v74, 0
	v_fmac_f32_e32 v5, v115, v67
	v_fmac_f32_e32 v14, v115, v75
	ds_read_b128 v[106:109], v6 offset:784
	ds_read_b128 v[110:113], v6 offset:1040
	s_waitcnt vmcnt(61)
; __device__ void adaln_partial_task(KParams& p, int task, float* sm) {
;     ...
;     for (int k = 0; k < 64; ++k) {
;       a0 += sc[k] * wv[k]; a1 += sc[64 + k] * wv[k]; a2 += sc[128 + k] * wv[k]; a3 += sc[192 + k] * wv[k]; a4 += sc[256 + k] * wv[k];
	v_fmac_f32_e32 v5, v116, v68
	v_fmac_f32_e32 v14, v116, v76
	s_waitcnt lgkmcnt(6)
	v_fma_f32 v15, v114, v86, 0
	s_waitcnt lgkmcnt(4)
	v_fma_f32 v12, v114, v94, 0
	s_waitcnt lgkmcnt(3)
	v_fma_f32 v10, v114, v98, 0
	s_waitcnt vmcnt(60)
	v_fmac_f32_e32 v5, v117, v69
	v_fmac_f32_e32 v14, v117, v77
	v_fmac_f32_e32 v15, v115, v87
	v_fmac_f32_e32 v12, v115, v95
	v_fmac_f32_e32 v10, v115, v99
	s_waitcnt vmcnt(59)
	v_fmac_f32_e32 v5, v118, v70
	v_fmac_f32_e32 v14, v118, v90
	v_fmac_f32_e32 v15, v116, v88
	v_fmac_f32_e32 v12, v116, v96
	v_fmac_f32_e32 v10, v116, v100
	s_waitcnt vmcnt(58)
	v_fmac_f32_e32 v5, v119, v71
	v_fmac_f32_e32 v14, v119, v91
	v_fmac_f32_e32 v15, v117, v89
	v_fmac_f32_e32 v12, v117, v97
	v_fmac_f32_e32 v10, v117, v101
	s_waitcnt vmcnt(57)
	v_fmac_f32_e32 v5, v120, v72
	v_fmac_f32_e32 v14, v120, v92
	ds_read_b128 v[66:69], v6 offset:288
	s_waitcnt lgkmcnt(3)
	v_fmac_f32_e32 v15, v118, v102
	s_waitcnt lgkmcnt(2)
	v_fmac_f32_e32 v12, v118, v106
	s_waitcnt lgkmcnt(1)
	v_fmac_f32_e32 v10, v118, v110
	s_waitcnt vmcnt(56)
	v_fmac_f32_e32 v5, v121, v73
	v_fmac_f32_e32 v14, v121, v93
	ds_read_b128 v[70:73], v6 offset:544
	ds_read_b128 v[74:77], v6 offset:304
	ds_read_b128 v[86:89], v6 offset:800
	ds_read_b128 v[90:93], v6 offset:1056
	ds_read_b128 v[94:97], v6 offset:560
	v_fmac_f32_e32 v15, v119, v103
	v_fmac_f32_e32 v12, v119, v107
	v_fmac_f32_e32 v10, v119, v111
	v_fmac_f32_e32 v15, v120, v104
	v_fmac_f32_e32 v12, v120, v108
	v_fmac_f32_e32 v10, v120, v112
	v_fmac_f32_e32 v15, v121, v105
	v_fmac_f32_e32 v12, v121, v109
	v_fmac_f32_e32 v10, v121, v113
	ds_read_b128 v[98:101], v6 offset:816
	ds_read_b128 v[102:105], v6 offset:1072
	s_waitcnt vmcnt(55)
	v_fmac_f32_e32 v5, v65, v78
	s_waitcnt lgkmcnt(7)
	v_fmac_f32_e32 v14, v65, v66
	s_waitcnt lgkmcnt(6)
	v_fmac_f32_e32 v15, v65, v70
	s_waitcnt lgkmcnt(4)
	v_fmac_f32_e32 v12, v65, v86
	s_waitcnt lgkmcnt(3)
	v_fmac_f32_e32 v10, v65, v90
	s_waitcnt vmcnt(54)
	v_fmac_f32_e32 v5, v64, v79
	v_fmac_f32_e32 v14, v64, v67
	v_fmac_f32_e32 v15, v64, v71
	v_fmac_f32_e32 v12, v64, v87
	v_fmac_f32_e32 v10, v64, v91
	s_waitcnt vmcnt(53)
	v_fmac_f32_e32 v5, v63, v80
	v_fmac_f32_e32 v14, v63, v68
	v_fmac_f32_e32 v15, v63, v72
	v_fmac_f32_e32 v12, v63, v88
	v_fmac_f32_e32 v10, v63, v92
	s_waitcnt vmcnt(52)
	v_fmac_f32_e32 v5, v62, v81
	v_fmac_f32_e32 v14, v62, v69
	v_fmac_f32_e32 v15, v62, v73
	v_fmac_f32_e32 v12, v62, v89
	v_fmac_f32_e32 v10, v62, v93
	s_waitcnt vmcnt(51)
	v_fmac_f32_e32 v5, v61, v82
	v_fmac_f32_e32 v14, v61, v74
	s_waitcnt lgkmcnt(2)
	v_fmac_f32_e32 v15, v61, v94
	s_waitcnt lgkmcnt(1)
	v_fmac_f32_e32 v12, v61, v98
	s_waitcnt lgkmcnt(0)
	v_fmac_f32_e32 v10, v61, v102
	s_waitcnt vmcnt(50)
	v_fmac_f32_e32 v5, v60, v83
	v_fmac_f32_e32 v14, v60, v75
	v_fmac_f32_e32 v15, v60, v95
	v_fmac_f32_e32 v12, v60, v99
	v_fmac_f32_e32 v10, v60, v103
	ds_read_b128 v[60:63], v6 offset:64
	s_waitcnt vmcnt(49)
	v_fmac_f32_e32 v5, v59, v84
	v_fmac_f32_e32 v14, v59, v76
	ds_read_b128 v[64:67], v6 offset:320
	ds_read_b128 v[68:71], v6 offset:80
	s_waitcnt vmcnt(48)
	v_fmac_f32_e32 v5, v58, v85
	v_fmac_f32_e32 v14, v58, v77
	ds_read_b128 v[72:75], v6 offset:576
	ds_read_b128 v[76:79], v6 offset:336
	ds_read_b128 v[80:83], v6 offset:832
	ds_read_b128 v[84:87], v6 offset:1088
	ds_read_b128 v[88:91], v6 offset:592
	v_fmac_f32_e32 v15, v59, v96
	v_fmac_f32_e32 v12, v59, v100
	v_fmac_f32_e32 v10, v59, v104
	v_fmac_f32_e32 v15, v58, v97
	v_fmac_f32_e32 v12, v58, v101
	v_fmac_f32_e32 v10, v58, v105
	s_waitcnt vmcnt(47) lgkmcnt(7)
	v_fmac_f32_e32 v5, v57, v60
	s_waitcnt lgkmcnt(6)
	v_fmac_f32_e32 v14, v57, v64
	ds_read_b128 v[92:95], v6 offset:848
	ds_read_b128 v[96:99], v6 offset:1104
	s_waitcnt lgkmcnt(6)
	v_fmac_f32_e32 v15, v57, v72
	s_waitcnt lgkmcnt(4)
	v_fmac_f32_e32 v12, v57, v80
	s_waitcnt lgkmcnt(3)
	v_fmac_f32_e32 v10, v57, v84
	s_waitcnt vmcnt(46)
	v_fmac_f32_e32 v5, v56, v61
	v_fmac_f32_e32 v14, v56, v65
	v_fmac_f32_e32 v15, v56, v73
	v_fmac_f32_e32 v12, v56, v81
	v_fmac_f32_e32 v10, v56, v85
	s_waitcnt vmcnt(45)
	v_fmac_f32_e32 v5, v55, v62
	v_fmac_f32_e32 v14, v55, v66
	v_fmac_f32_e32 v15, v55, v74
	v_fmac_f32_e32 v12, v55, v82
	v_fmac_f32_e32 v10, v55, v86
	s_waitcnt vmcnt(44)
	v_fmac_f32_e32 v5, v54, v63
	v_fmac_f32_e32 v14, v54, v67
	v_fmac_f32_e32 v15, v54, v75
	v_fmac_f32_e32 v12, v54, v83
	v_fmac_f32_e32 v10, v54, v87
	s_waitcnt vmcnt(43)
	v_fmac_f32_e32 v5, v53, v68
	v_fmac_f32_e32 v14, v53, v76
	s_waitcnt lgkmcnt(2)
	v_fmac_f32_e32 v15, v53, v88
	s_waitcnt lgkmcnt(1)
	v_fmac_f32_e32 v12, v53, v92
	s_waitcnt lgkmcnt(0)
	v_fmac_f32_e32 v10, v53, v96
	s_waitcnt vmcnt(42)
	v_fmac_f32_e32 v5, v52, v69
	v_fmac_f32_e32 v14, v52, v77
	v_fmac_f32_e32 v15, v52, v89
	v_fmac_f32_e32 v12, v52, v93
	v_fmac_f32_e32 v10, v52, v97
	s_waitcnt vmcnt(41)
	v_fmac_f32_e32 v5, v51, v70
	v_fmac_f32_e32 v14, v51, v78
	ds_read_b128 v[52:55], v6 offset:96
	s_waitcnt vmcnt(40)
	v_fmac_f32_e32 v5, v50, v71
	v_fmac_f32_e32 v14, v50, v79
	ds_read_b128 v[56:59], v6 offset:352
	ds_read_b128 v[60:63], v6 offset:112
	ds_read_b128 v[64:67], v6 offset:608
	ds_read_b128 v[68:71], v6 offset:368
	ds_read_b128 v[72:75], v6 offset:864
	ds_read_b128 v[76:79], v6 offset:1120
	ds_read_b128 v[80:83], v6 offset:624
	v_fmac_f32_e32 v15, v51, v90
	v_fmac_f32_e32 v12, v51, v94
	v_fmac_f32_e32 v10, v51, v98
	v_fmac_f32_e32 v15, v50, v91
	v_fmac_f32_e32 v12, v50, v95
	v_fmac_f32_e32 v10, v50, v99
	ds_read_b128 v[84:87], v6 offset:880
	ds_read_b128 v[88:91], v6 offset:1136
	s_waitcnt vmcnt(39) lgkmcnt(9)
	v_fmac_f32_e32 v5, v49, v52
	s_waitcnt lgkmcnt(8)
	v_fmac_f32_e32 v14, v49, v56
	s_waitcnt lgkmcnt(6)
	v_fmac_f32_e32 v15, v49, v64
	s_waitcnt lgkmcnt(4)
; __device__ void adaln_partial_task(KParams& p, int task, float* sm) {
;     ...
;     for (int k = 0; k < 64; ++k) {
;       a0 += sc[k] * wv[k]; a1 += sc[64 + k] * wv[k]; a2 += sc[128 + k] * wv[k]; a3 += sc[192 + k] * wv[k]; a4 += sc[256 + k] * wv[k];
	v_fmac_f32_e32 v12, v49, v72
	s_waitcnt lgkmcnt(3)
	v_fmac_f32_e32 v10, v49, v76
	s_waitcnt vmcnt(38)
	v_fmac_f32_e32 v5, v48, v53
	v_fmac_f32_e32 v14, v48, v57
	v_fmac_f32_e32 v15, v48, v65
	v_fmac_f32_e32 v12, v48, v73
	v_fmac_f32_e32 v10, v48, v77
	s_waitcnt vmcnt(37)
	v_fmac_f32_e32 v5, v47, v54
	v_fmac_f32_e32 v14, v47, v58
	v_fmac_f32_e32 v15, v47, v66
	v_fmac_f32_e32 v12, v47, v74
	v_fmac_f32_e32 v10, v47, v78
	s_waitcnt vmcnt(36)
	v_fmac_f32_e32 v5, v46, v55
	v_fmac_f32_e32 v14, v46, v59
	v_fmac_f32_e32 v15, v46, v67
	v_fmac_f32_e32 v12, v46, v75
	v_fmac_f32_e32 v10, v46, v79
	s_waitcnt vmcnt(35)
	v_fmac_f32_e32 v5, v45, v60
	v_fmac_f32_e32 v14, v45, v68
	s_waitcnt lgkmcnt(2)
	v_fmac_f32_e32 v15, v45, v80
	s_waitcnt lgkmcnt(1)
	v_fmac_f32_e32 v12, v45, v84
	s_waitcnt lgkmcnt(0)
	v_fmac_f32_e32 v10, v45, v88
	s_waitcnt vmcnt(34)
	v_fmac_f32_e32 v5, v44, v61
	v_fmac_f32_e32 v14, v44, v69
	v_fmac_f32_e32 v15, v44, v81
	v_fmac_f32_e32 v12, v44, v85
	v_fmac_f32_e32 v10, v44, v89
	ds_read_b128 v[44:47], v6 offset:128
	s_waitcnt vmcnt(33)
	v_fmac_f32_e32 v5, v43, v62
	v_fmac_f32_e32 v14, v43, v70
	ds_read_b128 v[48:51], v6 offset:384
	ds_read_b128 v[52:55], v6 offset:144
	s_waitcnt vmcnt(32)
	v_fmac_f32_e32 v5, v42, v63
	v_fmac_f32_e32 v14, v42, v71
	ds_read_b128 v[56:59], v6 offset:640
	ds_read_b128 v[60:63], v6 offset:400
	ds_read_b128 v[64:67], v6 offset:896
	ds_read_b128 v[68:71], v6 offset:1152
	ds_read_b128 v[72:75], v6 offset:656
	v_fmac_f32_e32 v15, v43, v82
	v_fmac_f32_e32 v12, v43, v86
	v_fmac_f32_e32 v10, v43, v90
	v_fmac_f32_e32 v15, v42, v83
	v_fmac_f32_e32 v12, v42, v87
	v_fmac_f32_e32 v10, v42, v91
	s_waitcnt vmcnt(31) lgkmcnt(7)
	v_fmac_f32_e32 v5, v41, v44
	s_waitcnt lgkmcnt(6)
	v_fmac_f32_e32 v14, v41, v48
	ds_read_b128 v[76:79], v6 offset:912
	ds_read_b128 v[80:83], v6 offset:1168
	s_waitcnt lgkmcnt(6)
	v_fmac_f32_e32 v15, v41, v56
	s_waitcnt lgkmcnt(4)
	v_fmac_f32_e32 v12, v41, v64
	s_waitcnt lgkmcnt(3)
	v_fmac_f32_e32 v10, v41, v68
	s_waitcnt vmcnt(30)
	v_fmac_f32_e32 v5, v40, v45
	v_fmac_f32_e32 v14, v40, v49
	v_fmac_f32_e32 v15, v40, v57
	v_fmac_f32_e32 v12, v40, v65
	v_fmac_f32_e32 v10, v40, v69
	s_waitcnt vmcnt(29)
	v_fmac_f32_e32 v5, v39, v46
	v_fmac_f32_e32 v14, v39, v50
	v_fmac_f32_e32 v15, v39, v58
	v_fmac_f32_e32 v12, v39, v66
	v_fmac_f32_e32 v10, v39, v70
	s_waitcnt vmcnt(28)
	v_fmac_f32_e32 v5, v38, v47
	v_fmac_f32_e32 v14, v38, v51
	v_fmac_f32_e32 v15, v38, v59
	v_fmac_f32_e32 v12, v38, v67
	v_fmac_f32_e32 v10, v38, v71
	s_waitcnt vmcnt(27)
	v_fmac_f32_e32 v5, v37, v52
	v_fmac_f32_e32 v14, v37, v60
	s_waitcnt lgkmcnt(2)
	v_fmac_f32_e32 v15, v37, v72
	s_waitcnt lgkmcnt(1)
	v_fmac_f32_e32 v12, v37, v76
	s_waitcnt lgkmcnt(0)
	v_fmac_f32_e32 v10, v37, v80
	s_waitcnt vmcnt(26)
	v_fmac_f32_e32 v5, v36, v53
	v_fmac_f32_e32 v14, v36, v61
	v_fmac_f32_e32 v15, v36, v73
	v_fmac_f32_e32 v12, v36, v77
	v_fmac_f32_e32 v10, v36, v81
	s_waitcnt vmcnt(25)
	v_fmac_f32_e32 v5, v35, v54
	v_fmac_f32_e32 v14, v35, v62
	ds_read_b128 v[36:39], v6 offset:160
	s_waitcnt vmcnt(24)
	v_fmac_f32_e32 v5, v34, v55
	v_fmac_f32_e32 v14, v34, v63
	ds_read_b128 v[40:43], v6 offset:416
	ds_read_b128 v[44:47], v6 offset:176
	ds_read_b128 v[48:51], v6 offset:672
	ds_read_b128 v[52:55], v6 offset:432
	ds_read_b128 v[56:59], v6 offset:928
	ds_read_b128 v[60:63], v6 offset:1184
	ds_read_b128 v[64:67], v6 offset:688
	v_fmac_f32_e32 v15, v35, v74
	v_fmac_f32_e32 v12, v35, v78
	v_fmac_f32_e32 v10, v35, v82
	v_fmac_f32_e32 v15, v34, v75
	v_fmac_f32_e32 v12, v34, v79
	v_fmac_f32_e32 v10, v34, v83
	ds_read_b128 v[68:71], v6 offset:944
	ds_read_b128 v[72:75], v6 offset:1200
	s_waitcnt vmcnt(23) lgkmcnt(9)
	v_fmac_f32_e32 v5, v33, v36
	s_waitcnt lgkmcnt(8)
	v_fmac_f32_e32 v14, v33, v40
	s_waitcnt lgkmcnt(6)
	v_fmac_f32_e32 v15, v33, v48
	s_waitcnt lgkmcnt(4)
	v_fmac_f32_e32 v12, v33, v56
	s_waitcnt lgkmcnt(3)
	v_fmac_f32_e32 v10, v33, v60
	s_waitcnt vmcnt(22)
	v_fmac_f32_e32 v5, v32, v37
	v_fmac_f32_e32 v14, v32, v41
	v_fmac_f32_e32 v15, v32, v49
	v_fmac_f32_e32 v12, v32, v57
	v_fmac_f32_e32 v10, v32, v61
	s_waitcnt vmcnt(21)
	v_fmac_f32_e32 v5, v31, v38
	v_fmac_f32_e32 v14, v31, v42
	v_fmac_f32_e32 v15, v31, v50
	v_fmac_f32_e32 v12, v31, v58
	v_fmac_f32_e32 v10, v31, v62
	s_waitcnt vmcnt(20)
	v_fmac_f32_e32 v5, v30, v39
	v_fmac_f32_e32 v14, v30, v43
	v_fmac_f32_e32 v15, v30, v51
	v_fmac_f32_e32 v12, v30, v59
	v_fmac_f32_e32 v10, v30, v63
	s_waitcnt vmcnt(19)
	v_fmac_f32_e32 v5, v29, v44
	v_fmac_f32_e32 v14, v29, v52
	s_waitcnt lgkmcnt(2)
	v_fmac_f32_e32 v15, v29, v64
	s_waitcnt lgkmcnt(1)
	v_fmac_f32_e32 v12, v29, v68
	s_waitcnt lgkmcnt(0)
	v_fmac_f32_e32 v10, v29, v72
	s_waitcnt vmcnt(18)
; __device__ void adaln_partial_task(KParams& p, int task, float* sm) {
;     ...
;     for (int k = 0; k < 64; ++k) {
;       a0 += sc[k] * wv[k]; a1 += sc[64 + k] * wv[k]; a2 += sc[128 + k] * wv[k]; a3 += sc[192 + k] * wv[k]; a4 += sc[256 + k] * wv[k];
;     }
;   }
;   float* pp = p.partial + (size_t)ks * 5 * NMOD + col;
;   pp[0] = a0; pp[NMOD] = a1; pp[2 * NMOD] = a2; pp[3 * NMOD] = a3; pp[4 * NMOD] = a4;
	v_fmac_f32_e32 v5, v28, v45
	v_fmac_f32_e32 v14, v28, v53
	v_fmac_f32_e32 v15, v28, v65
	v_fmac_f32_e32 v12, v28, v69
	v_fmac_f32_e32 v10, v28, v73
	ds_read_b128 v[28:31], v6 offset:192
	s_waitcnt vmcnt(17)
	v_fmac_f32_e32 v5, v27, v46
	v_fmac_f32_e32 v14, v27, v54
	ds_read_b128 v[32:35], v6 offset:448
	ds_read_b128 v[36:39], v6 offset:208
	s_waitcnt vmcnt(16)
	v_fmac_f32_e32 v5, v26, v47
	v_fmac_f32_e32 v14, v26, v55
	ds_read_b128 v[40:43], v6 offset:704
	ds_read_b128 v[44:47], v6 offset:464
	ds_read_b128 v[48:51], v6 offset:960
	ds_read_b128 v[52:55], v6 offset:1216
	ds_read_b128 v[56:59], v6 offset:720
	v_fmac_f32_e32 v15, v27, v66
	v_fmac_f32_e32 v12, v27, v70
	v_fmac_f32_e32 v10, v27, v74
	v_fmac_f32_e32 v15, v26, v67
	v_fmac_f32_e32 v12, v26, v71
	v_fmac_f32_e32 v10, v26, v75
	s_waitcnt vmcnt(15) lgkmcnt(7)
	v_fmac_f32_e32 v5, v25, v28
	s_waitcnt lgkmcnt(6)
	v_fmac_f32_e32 v14, v25, v32
	ds_read_b128 v[60:63], v6 offset:976
	ds_read_b128 v[64:67], v6 offset:1232
	s_waitcnt lgkmcnt(6)
	v_fmac_f32_e32 v15, v25, v40
	s_waitcnt lgkmcnt(4)
	v_fmac_f32_e32 v12, v25, v48
	s_waitcnt lgkmcnt(3)
	v_fmac_f32_e32 v10, v25, v52
	s_waitcnt vmcnt(14)
	v_fmac_f32_e32 v5, v24, v29
	v_fmac_f32_e32 v14, v24, v33
	v_fmac_f32_e32 v15, v24, v41
	v_fmac_f32_e32 v12, v24, v49
	v_fmac_f32_e32 v10, v24, v53
	s_waitcnt vmcnt(13)
	v_fmac_f32_e32 v5, v23, v30
	v_fmac_f32_e32 v14, v23, v34
	v_fmac_f32_e32 v15, v23, v42
	v_fmac_f32_e32 v12, v23, v50
	v_fmac_f32_e32 v10, v23, v54
	s_waitcnt vmcnt(12)
	v_fmac_f32_e32 v5, v22, v31
	v_fmac_f32_e32 v14, v22, v35
	v_fmac_f32_e32 v15, v22, v43
	v_fmac_f32_e32 v12, v22, v51
	v_fmac_f32_e32 v10, v22, v55
	s_waitcnt vmcnt(11)
	v_fmac_f32_e32 v5, v21, v36
	v_fmac_f32_e32 v14, v21, v44
	s_waitcnt lgkmcnt(2)
	v_fmac_f32_e32 v15, v21, v56
	s_waitcnt lgkmcnt(1)
	v_fmac_f32_e32 v12, v21, v60
	s_waitcnt lgkmcnt(0)
	v_fmac_f32_e32 v10, v21, v64
	s_waitcnt vmcnt(10)
	v_fmac_f32_e32 v5, v20, v37
	v_fmac_f32_e32 v14, v20, v45
	v_fmac_f32_e32 v15, v20, v57
	v_fmac_f32_e32 v12, v20, v61
	v_fmac_f32_e32 v10, v20, v65
	s_waitcnt vmcnt(9)
	v_fmac_f32_e32 v5, v19, v38
	v_fmac_f32_e32 v14, v19, v46
	ds_read_b128 v[20:23], v6 offset:224
	s_waitcnt vmcnt(8)
	v_fmac_f32_e32 v5, v18, v39
	v_fmac_f32_e32 v14, v18, v47
	ds_read_b128 v[24:27], v6 offset:480
	ds_read_b128 v[28:31], v6 offset:240
	ds_read_b128 v[32:35], v6 offset:736
	ds_read_b128 v[36:39], v6 offset:496
	ds_read_b128 v[40:43], v6 offset:992
	ds_read_b128 v[44:47], v6 offset:1248
	ds_read_b128 v[48:51], v6 offset:752
	v_fmac_f32_e32 v15, v19, v58
	v_fmac_f32_e32 v12, v19, v62
	v_fmac_f32_e32 v10, v19, v66
	v_fmac_f32_e32 v15, v18, v59
	v_fmac_f32_e32 v12, v18, v63
	v_fmac_f32_e32 v10, v18, v67
	ds_read_b128 v[52:55], v6 offset:1008
	ds_read_b128 v[56:59], v6 offset:1264
	s_waitcnt vmcnt(7) lgkmcnt(9)
	v_fmac_f32_e32 v5, v17, v20
	s_waitcnt lgkmcnt(8)
	v_fmac_f32_e32 v14, v17, v24
	s_waitcnt lgkmcnt(6)
	v_fmac_f32_e32 v15, v17, v32
	s_waitcnt lgkmcnt(4)
	v_fmac_f32_e32 v12, v17, v40
	s_waitcnt lgkmcnt(3)
	v_fmac_f32_e32 v10, v17, v44
	s_waitcnt vmcnt(6)
	v_fmac_f32_e32 v5, v16, v21
	v_fmac_f32_e32 v14, v16, v25
	v_fmac_f32_e32 v15, v16, v33
	v_fmac_f32_e32 v12, v16, v41
	v_fmac_f32_e32 v10, v16, v45
	s_waitcnt vmcnt(5)
	v_fmac_f32_e32 v5, v13, v22
	v_fmac_f32_e32 v14, v13, v26
	v_fmac_f32_e32 v15, v13, v34
	v_fmac_f32_e32 v12, v13, v42
	v_fmac_f32_e32 v10, v13, v46
	s_waitcnt vmcnt(4)
	v_fmac_f32_e32 v5, v11, v23
	v_fmac_f32_e32 v14, v11, v27
	v_fmac_f32_e32 v15, v11, v35
	v_fmac_f32_e32 v12, v11, v43
	v_fmac_f32_e32 v10, v11, v47
	s_waitcnt vmcnt(3)
	v_fmac_f32_e32 v5, v9, v28
	v_fmac_f32_e32 v14, v9, v36
	s_waitcnt lgkmcnt(2)
	v_fmac_f32_e32 v15, v9, v48
	s_waitcnt lgkmcnt(1)
	v_fmac_f32_e32 v12, v9, v52
	s_waitcnt lgkmcnt(0)
	v_fmac_f32_e32 v10, v9, v56
	s_waitcnt vmcnt(2)
	v_fmac_f32_e32 v5, v8, v29
	v_fmac_f32_e32 v14, v8, v37
	v_fmac_f32_e32 v15, v8, v49
	v_fmac_f32_e32 v12, v8, v53
	v_fmac_f32_e32 v10, v8, v57
	s_waitcnt vmcnt(1)
	v_fmac_f32_e32 v5, v7, v30
	v_fmac_f32_e32 v14, v7, v38
	v_fmac_f32_e32 v15, v7, v50
	v_fmac_f32_e32 v12, v7, v54
	v_fmac_f32_e32 v10, v7, v58
	s_waitcnt vmcnt(0)
	v_fmac_f32_e32 v5, v4, v31
	v_fmac_f32_e32 v14, v4, v39
	v_fmac_f32_e32 v15, v4, v51
	v_fmac_f32_e32 v12, v4, v55
	v_fmac_f32_e32 v10, v4, v59
	v_add_co_u32_e32 v4, vcc, s22, v2
	global_store_dword v[2:3], v5, off
	s_nop 0
	v_addc_co_u32_e32 v5, vcc, 0, v3, vcc
	global_store_dword v[4:5], v14, off
	v_add_co_u32_e32 v4, vcc, 0x18000, v2
	s_nop 1
	v_addc_co_u32_e32 v5, vcc, 0, v3, vcc
	global_store_dword v[4:5], v15, off
	v_add_co_u32_e32 v4, vcc, 0x24000, v2
	s_nop 1
	v_addc_co_u32_e32 v5, vcc, 0, v3, vcc
	v_add_co_u32_e32 v2, vcc, 0x30000, v2
	global_store_dword v[4:5], v12, off
	s_nop 0
	v_addc_co_u32_e32 v3, vcc, 0, v3, vcc
	global_store_dword v[2:3], v10, off
	s_cbranch_scc1 .LBB0_19
